# adds: conversion item loops keep the next item's 32 loads in flight through the LDS transpose (separate +32 wait ladder on the prefetching path)
# speedup vs baseline: 1.0341x; 1.0048x over previous
.LBB0_438:
	v_cvt_f32_u32_e32 v34, s83
	s_sub_i32 s54, 0, s83
	s_abs_i32 s7, s81
	s_ashr_i32 s6, s81, 31
	v_rcp_iflag_f32_e32 v34, v34
	s_nop 0
	v_mul_f32_e32 v34, 0x4f7ffffe, v34
	v_cvt_u32_f32_e32 v34, v34
	s_nop 0
	v_readfirstlane_b32 s55, v34
	s_mul_i32 s54, s54, s55
	s_mul_hi_u32 s54, s55, s54
	s_add_i32 s55, s55, s54
	s_mul_hi_u32 s54, s7, s55
	s_mul_i32 s55, s54, s83
	s_sub_i32 s7, s7, s55
	s_add_i32 s56, s54, 1
	s_sub_i32 s55, s7, s83
	s_cmp_ge_u32 s7, s83
	s_cselect_b32 s54, s56, s54
	s_cselect_b32 s7, s55, s7
	s_add_i32 s55, s54, 1
	s_cmp_ge_u32 s7, s83
	s_cselect_b32 s7, s55, s54
	s_xor_b32 s7, s7, s6
	s_sub_i32 s6, s7, s6
	s_mul_i32 s7, s6, s83
	s_lshl_b32 s6, s6, 6
	s_sub_i32 s7, s81, s7
	s_add_i32 s54, s26, -1
	v_or_b32_e32 v35, s6, v84
	s_ashr_i32 s6, s6, 31
	v_lshl_or_b32 v34, s7, 5, v1
	v_min_i32_e32 v34, s54, v34
	s_mul_i32 s54, s6, s26
	v_mad_u64_u32 v[36:37], s[6:7], v35, s26, 0
	v_add_u32_e32 v37, s54, v37
	s_waitcnt lgkmcnt(0)
	v_lshl_add_u64 v[36:37], v[36:37], 2, s[4:5]
	v_ashrrev_i32_e32 v35, 31, v34
	v_lshl_add_u64 v[34:35], v[34:35], 2, v[36:37]
	s_lshl_b64 s[4:5], s[26:27], 3
	v_lshl_add_u64 v[36:37], v[34:35], 0, s[4:5]
	v_lshl_add_u64 v[38:39], v[36:37], 0, s[4:5]
	v_lshl_add_u64 v[40:41], v[38:39], 0, s[4:5]
	v_lshl_add_u64 v[42:43], v[40:41], 0, s[4:5]
	v_lshl_add_u64 v[44:45], v[42:43], 0, s[4:5]
	v_lshl_add_u64 v[46:47], v[44:45], 0, s[4:5]
	v_lshl_add_u64 v[48:49], v[46:47], 0, s[4:5]
	global_load_dword v34, v[34:35], off nt
	s_nop 0
	global_load_dword v35, v[36:37], off nt
	s_nop 0
	global_load_dword v36, v[38:39], off nt
	global_load_dword v37, v[40:41], off nt
	s_nop 0
	global_load_dword v38, v[42:43], off nt
	global_load_dword v39, v[44:45], off nt
	global_load_dword v40, v[46:47], off nt
	global_load_dword v41, v[48:49], off nt
	v_lshl_add_u64 v[44:45], v[48:49], 0, s[4:5]
	global_load_dword v42, v[44:45], off nt
	v_lshl_add_u64 v[44:45], v[44:45], 0, s[4:5]
	v_lshl_add_u64 v[46:47], v[44:45], 0, s[4:5]
	global_load_dword v43, v[44:45], off nt
	s_nop 0
	global_load_dword v44, v[46:47], off nt
	v_lshl_add_u64 v[46:47], v[46:47], 0, s[4:5]
	v_lshl_add_u64 v[48:49], v[46:47], 0, s[4:5]
	global_load_dword v45, v[46:47], off nt
	s_nop 0
	global_load_dword v46, v[48:49], off nt
	v_lshl_add_u64 v[48:49], v[48:49], 0, s[4:5]
	v_lshl_add_u64 v[50:51], v[48:49], 0, s[4:5]
	global_load_dword v47, v[48:49], off nt
	s_nop 0
	global_load_dword v48, v[50:51], off nt
	v_lshl_add_u64 v[50:51], v[50:51], 0, s[4:5]
	v_lshl_add_u64 v[52:53], v[50:51], 0, s[4:5]
	global_load_dword v49, v[50:51], off nt
	s_nop 0
	global_load_dword v50, v[52:53], off nt
	v_lshl_add_u64 v[52:53], v[52:53], 0, s[4:5]
	v_lshl_add_u64 v[54:55], v[52:53], 0, s[4:5]
	global_load_dword v51, v[52:53], off nt
	s_nop 0
	global_load_dword v52, v[54:55], off nt
	v_lshl_add_u64 v[54:55], v[54:55], 0, s[4:5]
	v_lshl_add_u64 v[56:57], v[54:55], 0, s[4:5]
	global_load_dword v53, v[54:55], off nt
	s_nop 0
	global_load_dword v54, v[56:57], off nt
	v_lshl_add_u64 v[56:57], v[56:57], 0, s[4:5]
	v_lshl_add_u64 v[58:59], v[56:57], 0, s[4:5]
	global_load_dword v55, v[56:57], off nt
	s_nop 0
	global_load_dword v56, v[58:59], off nt
	v_lshl_add_u64 v[58:59], v[58:59], 0, s[4:5]
	v_lshl_add_u64 v[60:61], v[58:59], 0, s[4:5]
	global_load_dword v57, v[58:59], off nt
	s_nop 0
	global_load_dword v58, v[60:61], off nt
	v_lshl_add_u64 v[60:61], v[60:61], 0, s[4:5]
	v_lshl_add_u64 v[62:63], v[60:61], 0, s[4:5]
	global_load_dword v59, v[60:61], off nt
	s_nop 0
	global_load_dword v60, v[62:63], off nt
	v_lshl_add_u64 v[62:63], v[62:63], 0, s[4:5]
	v_lshl_add_u64 v[64:65], v[62:63], 0, s[4:5]
	global_load_dword v61, v[62:63], off nt
	s_nop 0
	global_load_dword v62, v[64:65], off nt
	v_lshl_add_u64 v[64:65], v[64:65], 0, s[4:5]
	v_lshl_add_u64 v[68:69], v[64:65], 0, s[4:5]
	global_load_dword v63, v[64:65], off nt
	s_nop 0
	global_load_dword v64, v[68:69], off nt
	v_lshl_add_u64 v[68:69], v[68:69], 0, s[4:5]
	global_load_dword v65, v[68:69], off nt
	s_abs_i32 s4, s3
	v_cvt_f32_u32_e32 v68, s4
	s_sub_i32 s7, 0, s4
	s_abs_i32 s6, s2
	s_xor_b32 s5, s2, s3
	v_rcp_iflag_f32_e32 v68, v68
	s_ashr_i32 s5, s5, 31
	s_waitcnt vmcnt(62)
	ds_write2_b32 v94, v2, v3 offset1:66
	s_waitcnt vmcnt(60)
	ds_write2_b32 v94, v4, v5 offset0:132 offset1:198
	v_mul_f32_e32 v68, 0x4f7ffffe, v68
	v_cvt_u32_f32_e32 v68, v68
	s_nop 0
	v_readfirstlane_b32 s54, v68
	s_mul_i32 s7, s7, s54
	s_mul_hi_u32 s7, s54, s7
	s_add_i32 s54, s54, s7
	s_mul_hi_u32 s7, s6, s54
	s_mul_i32 s54, s7, s4
	s_sub_i32 s6, s6, s54
	s_add_i32 s55, s7, 1
	s_sub_i32 s54, s6, s4
	s_cmp_ge_u32 s6, s4
	v_add_u32_e32 v68, 0x400, v94
	s_cselect_b32 s7, s55, s7
	s_waitcnt vmcnt(58)
	ds_write2_b32 v68, v6, v7 offset0:8 offset1:74
	s_waitcnt vmcnt(56)
	ds_write2_b32 v68, v8, v9 offset0:140 offset1:206
	v_add_u32_e32 v68, 0x800, v94
	s_cselect_b32 s6, s54, s6
	s_add_i32 s54, s7, 1
	s_waitcnt vmcnt(54)
	ds_write2_b32 v68, v10, v11 offset0:16 offset1:82
	s_waitcnt vmcnt(52)
	ds_write2_b32 v68, v12, v13 offset0:148 offset1:214
	v_add_u32_e32 v68, 0xc00, v94
	s_cmp_ge_u32 s6, s4
	s_waitcnt vmcnt(50)
	ds_write2_b32 v68, v14, v15 offset0:24 offset1:90
	s_waitcnt vmcnt(48)
	ds_write2_b32 v68, v16, v17 offset0:156 offset1:222
	v_add_u32_e32 v68, 0x1000, v94
	s_cselect_b32 s4, s54, s7
	s_waitcnt vmcnt(46)
	ds_write2_b32 v68, v18, v19 offset0:32 offset1:98
	s_waitcnt vmcnt(44)
	ds_write2_b32 v68, v20, v21 offset0:164 offset1:230
	v_add_u32_e32 v68, 0x1400, v94
	s_xor_b32 s4, s4, s5
	s_waitcnt vmcnt(42)
	ds_write2_b32 v68, v22, v23 offset0:40 offset1:106
	s_waitcnt vmcnt(40)
	ds_write2_b32 v68, v24, v25 offset0:172 offset1:238
	v_add_u32_e32 v68, 0x1800, v94
	s_sub_i32 s4, s4, s5
	s_waitcnt vmcnt(38)
	ds_write2_b32 v68, v26, v27 offset0:48 offset1:114
	s_waitcnt vmcnt(36)
	ds_write2_b32 v68, v28, v29 offset0:180 offset1:246
	v_add_u32_e32 v68, 0x1c00, v94
	s_mul_i32 s5, s4, s3
	s_waitcnt vmcnt(34)
	ds_write2_b32 v68, v30, v31 offset0:56 offset1:122
	s_waitcnt vmcnt(32)
	ds_write2_b32 v68, v32, v33 offset0:188 offset1:254
	s_branch .Lcv_cont_439

.Lcv_cont_439:
	s_sub_i32 s55, s2, s5
	s_waitcnt lgkmcnt(0)
	s_lshl_b32 s54, s4, 6
	s_lshl_b32 s85, s55, 5
	s_bitcmp0_b32 s55, 3
	s_movk_i32 s4, 0x400
	s_cselect_b32 s86, s4, 0xc00
	s_cmp_gt_i32 s33, 1
	s_mov_b64 s[4:5], -1
	s_cbranch_scc1 .LBB0_533
	ds_read2_b32 v[76:77], v87 offset1:33
	ds_read2_b32 v[74:75], v87 offset0:66 offset1:99
	ds_read2_b32 v[72:73], v87 offset0:132 offset1:165
	ds_read2_b32 v[70:71], v87 offset0:198 offset1:231
	s_cmp_lg_u32 s33, 1
	v_or_b32_e32 v79, s85, v85
	s_cselect_b64 s[6:7], -1, 0
	s_cmp_eq_u32 s33, 1
	s_cselect_b64 s[4:5], -1, 0
	v_cmp_lt_i32_e32 vcc, s71, v79
	s_and_b64 s[56:57], s[4:5], vcc
	v_mov_b32_e32 v78, v79
	s_and_saveexec_b64 s[4:5], s[56:57]
	s_cbranch_execz .LBB0_461
	s_cmpk_gt_u32 s85, 0x9ff
	s_mov_b64 s[56:57], -1
	s_cbranch_scc0 .LBB0_459
	s_cmpk_gt_u32 s85, 0xa2f
	s_cbranch_scc0 .LBB0_456
	s_cmpk_gt_u32 s85, 0xe2f
	s_cbranch_scc0 .LBB0_453
	s_cmpk_gt_u32 s85, 0x122f
	s_cbranch_scc0 .LBB0_450
	s_cmpk_gt_u32 s85, 0x1237
	s_cbranch_scc0 .LBB0_447
	v_add_u32_e32 v78, 0xc8, v79
	s_mov_b64 s[56:57], 0

.LBB0_589:
	s_waitcnt lgkmcnt(0)
	s_andn2_b64 vcc, exec, s[50:51]
	s_cbranch_vccnz .LBB0_394
	s_waitcnt vmcnt(0)
	v_mov_b64_e32 v[2:3], v[34:35]
	s_mov_b32 s3, s83
	s_mov_b32 s2, s81
	s_mov_b32 s33, s84
	s_mov_b32 s21, s82
	s_mov_b64 s[24:25], s[52:53]
	s_mov_b32 s79, s26
	v_mov_b64_e32 v[4:5], v[36:37]
	v_mov_b64_e32 v[6:7], v[38:39]
	v_mov_b64_e32 v[8:9], v[40:41]
	v_mov_b64_e32 v[10:11], v[42:43]
	v_mov_b64_e32 v[12:13], v[44:45]
	v_mov_b64_e32 v[14:15], v[46:47]
	v_mov_b64_e32 v[16:17], v[48:49]
	v_mov_b64_e32 v[18:19], v[50:51]
	v_mov_b64_e32 v[20:21], v[52:53]
	v_mov_b64_e32 v[22:23], v[54:55]
	v_mov_b64_e32 v[24:25], v[56:57]
	v_mov_b64_e32 v[26:27], v[58:59]
	v_mov_b64_e32 v[28:29], v[60:61]
	v_mov_b64_e32 v[30:31], v[62:63]
	v_mov_b64_e32 v[32:33], v[64:65]
	s_mov_b32 s1, s80
	s_branch .LBB0_394

.LBB0_811:
	v_cvt_f32_u32_e32 v34, s83
	s_sub_i32 s54, 0, s83
	s_abs_i32 s7, s81
	s_ashr_i32 s6, s81, 31
	v_rcp_iflag_f32_e32 v34, v34
	s_nop 0
	v_mul_f32_e32 v34, 0x4f7ffffe, v34
	v_cvt_u32_f32_e32 v34, v34
	s_nop 0
	v_readfirstlane_b32 s55, v34
	s_mul_i32 s54, s54, s55
	s_mul_hi_u32 s54, s55, s54
	s_add_i32 s55, s55, s54
	s_mul_hi_u32 s54, s7, s55
	s_mul_i32 s55, s54, s83
	s_sub_i32 s7, s7, s55
	s_add_i32 s56, s54, 1
	s_sub_i32 s55, s7, s83
	s_cmp_ge_u32 s7, s83
	s_cselect_b32 s54, s56, s54
	s_cselect_b32 s7, s55, s7
	s_add_i32 s55, s54, 1
	s_cmp_ge_u32 s7, s83
	s_cselect_b32 s7, s55, s54
	s_xor_b32 s7, s7, s6
	s_sub_i32 s6, s7, s6
	s_mul_i32 s7, s6, s83
	s_lshl_b32 s6, s6, 6
	s_sub_i32 s7, s81, s7
	s_add_i32 s54, s26, -1
	v_or_b32_e32 v35, s6, v84
	s_ashr_i32 s6, s6, 31
	v_lshl_or_b32 v34, s7, 5, v1
	v_min_i32_e32 v34, s54, v34
	s_mul_i32 s54, s6, s26
	v_mad_u64_u32 v[36:37], s[6:7], v35, s26, 0
	v_add_u32_e32 v37, s54, v37
	s_waitcnt lgkmcnt(0)
	v_lshl_add_u64 v[36:37], v[36:37], 2, s[4:5]
	v_ashrrev_i32_e32 v35, 31, v34
	v_lshl_add_u64 v[34:35], v[34:35], 2, v[36:37]
	s_lshl_b64 s[4:5], s[26:27], 3
	v_lshl_add_u64 v[36:37], v[34:35], 0, s[4:5]
	v_lshl_add_u64 v[38:39], v[36:37], 0, s[4:5]
	v_lshl_add_u64 v[40:41], v[38:39], 0, s[4:5]
	v_lshl_add_u64 v[42:43], v[40:41], 0, s[4:5]
	v_lshl_add_u64 v[44:45], v[42:43], 0, s[4:5]
	v_lshl_add_u64 v[46:47], v[44:45], 0, s[4:5]
	v_lshl_add_u64 v[48:49], v[46:47], 0, s[4:5]
	global_load_dword v34, v[34:35], off nt
	s_nop 0
	global_load_dword v35, v[36:37], off nt
	s_nop 0
	global_load_dword v36, v[38:39], off nt
	global_load_dword v37, v[40:41], off nt
	s_nop 0
	global_load_dword v38, v[42:43], off nt
	global_load_dword v39, v[44:45], off nt
	global_load_dword v40, v[46:47], off nt
	global_load_dword v41, v[48:49], off nt
	v_lshl_add_u64 v[44:45], v[48:49], 0, s[4:5]
	global_load_dword v42, v[44:45], off nt
	v_lshl_add_u64 v[44:45], v[44:45], 0, s[4:5]
	v_lshl_add_u64 v[46:47], v[44:45], 0, s[4:5]
	global_load_dword v43, v[44:45], off nt
	s_nop 0
	global_load_dword v44, v[46:47], off nt
	v_lshl_add_u64 v[46:47], v[46:47], 0, s[4:5]
	v_lshl_add_u64 v[48:49], v[46:47], 0, s[4:5]
	global_load_dword v45, v[46:47], off nt
	s_nop 0
	global_load_dword v46, v[48:49], off nt
	v_lshl_add_u64 v[48:49], v[48:49], 0, s[4:5]
	v_lshl_add_u64 v[50:51], v[48:49], 0, s[4:5]
	global_load_dword v47, v[48:49], off nt
	s_nop 0
	global_load_dword v48, v[50:51], off nt
	v_lshl_add_u64 v[50:51], v[50:51], 0, s[4:5]
	v_lshl_add_u64 v[52:53], v[50:51], 0, s[4:5]
	global_load_dword v49, v[50:51], off nt
	s_nop 0
	global_load_dword v50, v[52:53], off nt
	v_lshl_add_u64 v[52:53], v[52:53], 0, s[4:5]
	v_lshl_add_u64 v[54:55], v[52:53], 0, s[4:5]
	global_load_dword v51, v[52:53], off nt
	s_nop 0
	global_load_dword v52, v[54:55], off nt
	v_lshl_add_u64 v[54:55], v[54:55], 0, s[4:5]
	v_lshl_add_u64 v[56:57], v[54:55], 0, s[4:5]
	global_load_dword v53, v[54:55], off nt
	s_nop 0
	global_load_dword v54, v[56:57], off nt
	v_lshl_add_u64 v[56:57], v[56:57], 0, s[4:5]
	v_lshl_add_u64 v[58:59], v[56:57], 0, s[4:5]
	global_load_dword v55, v[56:57], off nt
	s_nop 0
	global_load_dword v56, v[58:59], off nt
	v_lshl_add_u64 v[58:59], v[58:59], 0, s[4:5]
	v_lshl_add_u64 v[60:61], v[58:59], 0, s[4:5]
	global_load_dword v57, v[58:59], off nt
	s_nop 0
	global_load_dword v58, v[60:61], off nt
	v_lshl_add_u64 v[60:61], v[60:61], 0, s[4:5]
	v_lshl_add_u64 v[62:63], v[60:61], 0, s[4:5]
	global_load_dword v59, v[60:61], off nt
	s_nop 0
	global_load_dword v60, v[62:63], off nt
	v_lshl_add_u64 v[62:63], v[62:63], 0, s[4:5]
	v_lshl_add_u64 v[64:65], v[62:63], 0, s[4:5]
	global_load_dword v61, v[62:63], off nt
	s_nop 0
	global_load_dword v62, v[64:65], off nt
	v_lshl_add_u64 v[64:65], v[64:65], 0, s[4:5]
	v_lshl_add_u64 v[68:69], v[64:65], 0, s[4:5]
	global_load_dword v63, v[64:65], off nt
	s_nop 0
	global_load_dword v64, v[68:69], off nt
	v_lshl_add_u64 v[68:69], v[68:69], 0, s[4:5]
	global_load_dword v65, v[68:69], off nt
	s_abs_i32 s4, s2
	v_cvt_f32_u32_e32 v68, s4
	s_sub_i32 s7, 0, s4
	s_abs_i32 s6, s1
	s_xor_b32 s5, s1, s2
	v_rcp_iflag_f32_e32 v68, v68
	s_ashr_i32 s5, s5, 31
	s_waitcnt vmcnt(62)
	ds_write2_b32 v94, v2, v3 offset1:66
	s_waitcnt vmcnt(60)
	ds_write2_b32 v94, v4, v5 offset0:132 offset1:198
	v_mul_f32_e32 v68, 0x4f7ffffe, v68
	v_cvt_u32_f32_e32 v68, v68
	s_nop 0
	v_readfirstlane_b32 s54, v68
	s_mul_i32 s7, s7, s54
	s_mul_hi_u32 s7, s54, s7
	s_add_i32 s54, s54, s7
	s_mul_hi_u32 s7, s6, s54
	s_mul_i32 s54, s7, s4
	s_sub_i32 s6, s6, s54
	s_add_i32 s55, s7, 1
	s_sub_i32 s54, s6, s4
	s_cmp_ge_u32 s6, s4
	v_add_u32_e32 v68, 0x400, v94
	s_cselect_b32 s7, s55, s7
	s_waitcnt vmcnt(58)
	ds_write2_b32 v68, v6, v7 offset0:8 offset1:74
	s_waitcnt vmcnt(56)
	ds_write2_b32 v68, v8, v9 offset0:140 offset1:206
	v_add_u32_e32 v68, 0x800, v94
	s_cselect_b32 s6, s54, s6
	s_add_i32 s54, s7, 1
	s_waitcnt vmcnt(54)
	ds_write2_b32 v68, v10, v11 offset0:16 offset1:82
	s_waitcnt vmcnt(52)
	ds_write2_b32 v68, v12, v13 offset0:148 offset1:214
	v_add_u32_e32 v68, 0xc00, v94
	s_cmp_ge_u32 s6, s4
	s_waitcnt vmcnt(50)
	ds_write2_b32 v68, v14, v15 offset0:24 offset1:90
	s_waitcnt vmcnt(48)
	ds_write2_b32 v68, v16, v17 offset0:156 offset1:222
	v_add_u32_e32 v68, 0x1000, v94
	s_cselect_b32 s4, s54, s7
	s_waitcnt vmcnt(46)
	ds_write2_b32 v68, v18, v19 offset0:32 offset1:98
	s_waitcnt vmcnt(44)
	ds_write2_b32 v68, v20, v21 offset0:164 offset1:230
	v_add_u32_e32 v68, 0x1400, v94
	s_xor_b32 s4, s4, s5
	s_waitcnt vmcnt(42)
	ds_write2_b32 v68, v22, v23 offset0:40 offset1:106
	s_waitcnt vmcnt(40)
	ds_write2_b32 v68, v24, v25 offset0:172 offset1:238
	v_add_u32_e32 v68, 0x1800, v94
	s_sub_i32 s4, s4, s5
	s_waitcnt vmcnt(38)
	ds_write2_b32 v68, v26, v27 offset0:48 offset1:114
	s_waitcnt vmcnt(36)
	ds_write2_b32 v68, v28, v29 offset0:180 offset1:246
	v_add_u32_e32 v68, 0x1c00, v94
	s_mul_i32 s5, s4, s2
	s_waitcnt vmcnt(34)
	ds_write2_b32 v68, v30, v31 offset0:56 offset1:122
	s_waitcnt vmcnt(32)
	ds_write2_b32 v68, v32, v33 offset0:188 offset1:254
	s_branch .Lcv_cont_812

.Lcv_cont_812:
	s_sub_i32 s55, s1, s5
	s_waitcnt lgkmcnt(0)
	s_lshl_b32 s54, s4, 6
	s_lshl_b32 s85, s55, 5
	s_bitcmp0_b32 s55, 3
	s_movk_i32 s4, 0x400
	s_cselect_b32 s86, s4, 0xc00
	s_cmp_gt_i32 s21, 1
	s_mov_b64 s[4:5], -1
	s_cbranch_scc1 .LBB0_906
	ds_read2_b32 v[76:77], v87 offset1:33
	ds_read2_b32 v[74:75], v87 offset0:66 offset1:99
	ds_read2_b32 v[72:73], v87 offset0:132 offset1:165
	ds_read2_b32 v[70:71], v87 offset0:198 offset1:231
	s_cmp_lg_u32 s21, 1
	v_or_b32_e32 v79, s85, v85
	s_cselect_b64 s[6:7], -1, 0
	s_cmp_eq_u32 s21, 1
	s_cselect_b64 s[4:5], -1, 0
	v_cmp_lt_i32_e32 vcc, s70, v79
	s_and_b64 s[56:57], s[4:5], vcc
	v_mov_b32_e32 v78, v79
	s_and_saveexec_b64 s[4:5], s[56:57]
	s_cbranch_execz .LBB0_834
	s_cmpk_gt_u32 s85, 0x9ff
	s_mov_b64 s[56:57], -1
	s_cbranch_scc0 .LBB0_832
	s_cmpk_gt_u32 s85, 0xa2f
	s_cbranch_scc0 .LBB0_829
	s_cmpk_gt_u32 s85, 0xe2f
	s_cbranch_scc0 .LBB0_826
	s_cmpk_gt_u32 s85, 0x122f
	s_cbranch_scc0 .LBB0_823
	s_cmpk_gt_u32 s85, 0x1237
	s_cbranch_scc0 .LBB0_820
	v_add_u32_e32 v78, 0xc8, v79
	s_mov_b64 s[56:57], 0

.LBB0_962:
	s_waitcnt lgkmcnt(0)
	s_andn2_b64 vcc, exec, s[50:51]
	s_cbranch_vccnz .LBB0_768
	s_waitcnt vmcnt(0)
	v_mov_b64_e32 v[2:3], v[34:35]
	s_mov_b32 s2, s83
	s_mov_b32 s1, s81
	s_mov_b32 s21, s84
	s_mov_b32 s3, s82
	s_mov_b64 s[24:25], s[52:53]
	s_mov_b32 s78, s26
	v_mov_b64_e32 v[4:5], v[36:37]
	v_mov_b64_e32 v[6:7], v[38:39]
	v_mov_b64_e32 v[8:9], v[40:41]
	v_mov_b64_e32 v[10:11], v[42:43]
	v_mov_b64_e32 v[12:13], v[44:45]
	v_mov_b64_e32 v[14:15], v[46:47]
	v_mov_b64_e32 v[16:17], v[48:49]
	v_mov_b64_e32 v[18:19], v[50:51]
	v_mov_b64_e32 v[20:21], v[52:53]
	v_mov_b64_e32 v[22:23], v[54:55]
	v_mov_b64_e32 v[24:25], v[56:57]
	v_mov_b64_e32 v[26:27], v[58:59]
	v_mov_b64_e32 v[28:29], v[60:61]
	v_mov_b64_e32 v[30:31], v[62:63]
	v_mov_b64_e32 v[32:33], v[64:65]
	s_mov_b32 s79, s80
	s_branch .LBB0_768

.LBB0_1605:
	v_cvt_f32_u32_e32 v36, s57
	s_sub_i32 s8, 0, s57
	s_abs_i32 s1, s55
	s_ashr_i32 s0, s55, 31
	v_rcp_iflag_f32_e32 v36, v36
	s_nop 0
	v_mul_f32_e32 v36, 0x4f7ffffe, v36
	v_cvt_u32_f32_e32 v36, v36
	s_nop 0
	v_readfirstlane_b32 s9, v36
	s_mul_i32 s8, s8, s9
	s_mul_hi_u32 s8, s9, s8
	s_add_i32 s9, s9, s8
	s_mul_hi_u32 s8, s1, s9
	s_mul_i32 s9, s8, s57
	s_sub_i32 s1, s1, s9
	s_add_i32 s9, s8, 1
	s_sub_i32 s36, s1, s57
	s_cmp_ge_u32 s1, s57
	s_cselect_b32 s8, s9, s8
	s_cselect_b32 s1, s36, s1
	s_add_i32 s9, s8, 1
	s_cmp_ge_u32 s1, s57
	s_cselect_b32 s1, s9, s8
	s_xor_b32 s1, s1, s0
	s_sub_i32 s0, s1, s0
	s_mul_i32 s1, s0, s57
	s_lshl_b32 s0, s0, 6
	s_sub_i32 s1, s55, s1
	v_or_b32_e32 v37, s0, v85
	s_ashr_i32 s0, s0, 31
	v_lshl_or_b32 v36, s1, 5, v84
	s_add_i32 s1, s68, -1
	s_mul_i32 s0, s0, s68
	v_mad_u64_u32 v[38:39], s[8:9], v37, s68, 0
	v_min_i32_e32 v36, s1, v36
	v_add_u32_e32 v39, s0, v39
	v_lshl_add_u64 v[38:39], v[38:39], 2, s[6:7]
	v_ashrrev_i32_e32 v37, 31, v36
	v_lshl_add_u64 v[38:39], v[36:37], 2, v[38:39]
	s_lshl_b64 s[6:7], s[68:69], 3
	global_load_dword v36, v[38:39], off nt
	v_lshl_add_u64 v[38:39], v[38:39], 0, s[6:7]
	v_lshl_add_u64 v[40:41], v[38:39], 0, s[6:7]
	global_load_dword v37, v[38:39], off nt
	s_nop 0
	global_load_dword v38, v[40:41], off nt
	v_lshl_add_u64 v[40:41], v[40:41], 0, s[6:7]
	v_lshl_add_u64 v[42:43], v[40:41], 0, s[6:7]
	global_load_dword v39, v[40:41], off nt
	s_nop 0
	global_load_dword v40, v[42:43], off nt
	v_lshl_add_u64 v[42:43], v[42:43], 0, s[6:7]
	v_lshl_add_u64 v[44:45], v[42:43], 0, s[6:7]
	global_load_dword v41, v[42:43], off nt
	s_nop 0
	global_load_dword v42, v[44:45], off nt
	v_lshl_add_u64 v[44:45], v[44:45], 0, s[6:7]
	v_lshl_add_u64 v[46:47], v[44:45], 0, s[6:7]
	global_load_dword v43, v[44:45], off nt
	s_nop 0
	global_load_dword v44, v[46:47], off nt
	v_lshl_add_u64 v[46:47], v[46:47], 0, s[6:7]
	v_lshl_add_u64 v[48:49], v[46:47], 0, s[6:7]
	global_load_dword v45, v[46:47], off nt
	s_nop 0
	global_load_dword v46, v[48:49], off nt
	v_lshl_add_u64 v[48:49], v[48:49], 0, s[6:7]
	v_lshl_add_u64 v[50:51], v[48:49], 0, s[6:7]
	global_load_dword v47, v[48:49], off nt
	s_nop 0
	global_load_dword v48, v[50:51], off nt
	v_lshl_add_u64 v[50:51], v[50:51], 0, s[6:7]
	v_lshl_add_u64 v[52:53], v[50:51], 0, s[6:7]
	global_load_dword v49, v[50:51], off nt
	s_nop 0
	global_load_dword v50, v[52:53], off nt
	v_lshl_add_u64 v[52:53], v[52:53], 0, s[6:7]
	v_lshl_add_u64 v[54:55], v[52:53], 0, s[6:7]
	global_load_dword v51, v[52:53], off nt
	s_nop 0
	global_load_dword v52, v[54:55], off nt
	v_lshl_add_u64 v[54:55], v[54:55], 0, s[6:7]
	v_lshl_add_u64 v[56:57], v[54:55], 0, s[6:7]
	global_load_dword v53, v[54:55], off nt
	s_nop 0
	global_load_dword v54, v[56:57], off nt
	v_lshl_add_u64 v[56:57], v[56:57], 0, s[6:7]
	v_lshl_add_u64 v[58:59], v[56:57], 0, s[6:7]
	global_load_dword v55, v[56:57], off nt
	s_nop 0
	global_load_dword v56, v[58:59], off nt
	v_lshl_add_u64 v[58:59], v[58:59], 0, s[6:7]
	v_lshl_add_u64 v[60:61], v[58:59], 0, s[6:7]
	global_load_dword v57, v[58:59], off nt
	s_nop 0
	global_load_dword v58, v[60:61], off nt
	v_lshl_add_u64 v[60:61], v[60:61], 0, s[6:7]
	v_lshl_add_u64 v[62:63], v[60:61], 0, s[6:7]
	global_load_dword v59, v[60:61], off nt
	s_nop 0
	global_load_dword v60, v[62:63], off nt
	v_lshl_add_u64 v[62:63], v[62:63], 0, s[6:7]
	v_lshl_add_u64 v[64:65], v[62:63], 0, s[6:7]
	global_load_dword v61, v[62:63], off nt
	s_nop 0
	global_load_dword v62, v[64:65], off nt
	v_lshl_add_u64 v[64:65], v[64:65], 0, s[6:7]
	v_lshl_add_u64 v[66:67], v[64:65], 0, s[6:7]
	global_load_dword v63, v[64:65], off nt
	s_nop 0
	global_load_dword v64, v[66:67], off nt
	v_lshl_add_u64 v[66:67], v[66:67], 0, s[6:7]
	s_waitcnt lgkmcnt(0)
	v_lshl_add_u64 v[68:69], v[66:67], 0, s[6:7]
	global_load_dword v65, v[66:67], off nt
	s_nop 0
	global_load_dword v66, v[68:69], off nt
	v_lshl_add_u64 v[68:69], v[68:69], 0, s[6:7]
	global_load_dword v67, v[68:69], off nt
	s_abs_i32 s0, s81
	s_waitcnt lgkmcnt(0)
	v_cvt_f32_u32_e32 v68, s0
	s_sub_i32 s7, 0, s0
	s_abs_i32 s6, s54
	s_xor_b32 s1, s54, s81
	v_rcp_iflag_f32_e32 v68, v68
	s_ashr_i32 s1, s1, 31
	s_waitcnt vmcnt(62)
	ds_write2_b32 v95, v4, v5 offset1:66
	s_waitcnt vmcnt(60)
	ds_write2_b32 v95, v6, v7 offset0:132 offset1:198
	v_mul_f32_e32 v68, 0x4f7ffffe, v68
	v_cvt_u32_f32_e32 v68, v68
	s_nop 0
	v_readfirstlane_b32 s8, v68
	s_mul_i32 s7, s7, s8
	s_mul_hi_u32 s7, s8, s7
	s_add_i32 s8, s8, s7
	s_mul_hi_u32 s7, s6, s8
	s_mul_i32 s8, s7, s0
	s_sub_i32 s6, s6, s8
	s_add_i32 s9, s7, 1
	s_sub_i32 s8, s6, s0
	s_cmp_ge_u32 s6, s0
	v_add_u32_e32 v68, 0x400, v95
	s_cselect_b32 s7, s9, s7
	s_waitcnt vmcnt(58)
	ds_write2_b32 v68, v8, v9 offset0:8 offset1:74
	s_waitcnt vmcnt(56)
	ds_write2_b32 v68, v10, v11 offset0:140 offset1:206
	v_add_u32_e32 v68, 0x800, v95
	s_cselect_b32 s6, s8, s6
	s_add_i32 s8, s7, 1
	s_waitcnt vmcnt(54)
	ds_write2_b32 v68, v12, v13 offset0:16 offset1:82
	s_waitcnt vmcnt(52)
	ds_write2_b32 v68, v14, v15 offset0:148 offset1:214
	v_add_u32_e32 v68, 0xc00, v95
	s_cmp_ge_u32 s6, s0
	s_waitcnt vmcnt(50)
	ds_write2_b32 v68, v16, v17 offset0:24 offset1:90
	s_waitcnt vmcnt(48)
	ds_write2_b32 v68, v18, v19 offset0:156 offset1:222
	v_add_u32_e32 v68, 0x1000, v95
	s_cselect_b32 s0, s8, s7
	s_waitcnt vmcnt(46)
	ds_write2_b32 v68, v20, v21 offset0:32 offset1:98
	s_waitcnt vmcnt(44)
	ds_write2_b32 v68, v22, v23 offset0:164 offset1:230
	v_add_u32_e32 v68, 0x1400, v95
	s_xor_b32 s0, s0, s1
	s_waitcnt vmcnt(42)
	ds_write2_b32 v68, v24, v25 offset0:40 offset1:106
	s_waitcnt vmcnt(40)
	ds_write2_b32 v68, v26, v27 offset0:172 offset1:238
	v_add_u32_e32 v68, 0x1800, v95
	s_sub_i32 s0, s0, s1
	s_waitcnt vmcnt(38)
	ds_write2_b32 v68, v28, v29 offset0:48 offset1:114
	s_waitcnt vmcnt(36)
	ds_write2_b32 v68, v30, v31 offset0:180 offset1:246
	v_add_u32_e32 v68, 0x1c00, v95
	s_mul_i32 s1, s0, s81
	s_waitcnt vmcnt(34)
	ds_write2_b32 v68, v32, v33 offset0:56 offset1:122
	s_waitcnt vmcnt(32)
	ds_write2_b32 v68, v34, v35 offset0:188 offset1:254
	s_branch .Lcv_cont_1606

.Lcv_cont_1606:
	s_sub_i32 s89, s54, s1
	s_waitcnt lgkmcnt(0)
	s_lshl_b32 s88, s0, 6
	s_lshl_b32 s58, s89, 5
	s_bitcmp0_b32 s89, 3
	s_cselect_b32 s59, 0x400, s17
	s_cmp_gt_i32 s25, 1
	s_mov_b64 s[6:7], -1
	s_cbranch_scc1 .LBB0_1700
	ds_read2_b32 v[76:77], v88 offset1:33
	ds_read2_b32 v[74:75], v88 offset0:66 offset1:99
	ds_read2_b32 v[72:73], v88 offset0:132 offset1:165
	ds_read2_b32 v[70:71], v88 offset0:198 offset1:231
	s_cmp_lg_u32 s25, 1
	v_or_b32_e32 v79, s58, v86
	s_cselect_b64 s[8:9], -1, 0
	s_cmp_eq_u32 s25, 1
	s_cselect_b64 s[6:7], -1, 0
	v_cmp_lt_i32_e32 vcc, s30, v79
	s_and_b64 s[36:37], s[6:7], vcc
	v_mov_b32_e32 v78, v79
	s_and_saveexec_b64 s[6:7], s[36:37]
	s_cbranch_execz .LBB0_1628
	s_cmpk_gt_u32 s58, 0x9ff
	s_mov_b64 s[36:37], -1
	s_cbranch_scc0 .LBB0_1626
	s_cmpk_gt_u32 s58, 0xa2f
	s_cbranch_scc0 .LBB0_1623
	s_cmpk_gt_u32 s58, 0xe2f
	s_cbranch_scc0 .LBB0_1620
	s_cmpk_gt_u32 s58, 0x122f
	s_cbranch_scc0 .LBB0_1617
	s_cmpk_gt_u32 s58, 0x1237
	s_cbranch_scc0 .LBB0_1614
	v_add_u32_e32 v78, 0xc8, v79
	s_mov_b64 s[36:37], 0

.LBB0_1756:
	s_waitcnt lgkmcnt(0)
	s_andn2_b64 vcc, exec, s[84:85]
	s_cbranch_vccnz .LBB0_1554
	s_waitcnt vmcnt(0)
	v_mov_b64_e32 v[4:5], v[36:37]
	s_mov_b32 s81, s57
	s_mov_b32 s54, s55
	s_mov_b32 s25, s29
	s_mov_b32 s24, s28
	s_mov_b64 s[10:11], s[86:87]
	s_mov_b32 s26, s68
	v_mov_b64_e32 v[6:7], v[38:39]
	v_mov_b64_e32 v[8:9], v[40:41]
	v_mov_b64_e32 v[10:11], v[42:43]
	v_mov_b64_e32 v[12:13], v[44:45]
	v_mov_b64_e32 v[14:15], v[46:47]
	v_mov_b64_e32 v[16:17], v[48:49]
	v_mov_b64_e32 v[18:19], v[50:51]
	v_mov_b64_e32 v[20:21], v[52:53]
	v_mov_b64_e32 v[22:23], v[54:55]
	v_mov_b64_e32 v[24:25], v[56:57]
	v_mov_b64_e32 v[26:27], v[58:59]
	v_mov_b64_e32 v[28:29], v[60:61]
	v_mov_b64_e32 v[30:31], v[62:63]
	v_mov_b64_e32 v[32:33], v[64:65]
	v_mov_b64_e32 v[34:35], v[66:67]
	s_mov_b32 s56, s27
	s_branch .LBB0_1554

.LBB0_2701:
	v_cvt_f32_u32_e32 v34, s37
	s_sub_i32 s6, 0, s37
	s_abs_i32 s3, s36
	s_ashr_i32 s2, s36, 31
	v_rcp_iflag_f32_e32 v34, v34
	s_nop 0
	v_mul_f32_e32 v34, 0x4f7ffffe, v34
	v_cvt_u32_f32_e32 v34, v34
	s_nop 0
	v_readfirstlane_b32 s7, v34
	s_mul_i32 s6, s6, s7
	s_mul_hi_u32 s6, s7, s6
	s_add_i32 s7, s7, s6
	s_mul_hi_u32 s6, s3, s7
	s_mul_i32 s7, s6, s37
	s_sub_i32 s3, s3, s7
	s_add_i32 s7, s6, 1
	s_sub_i32 s14, s3, s37
	s_cmp_ge_u32 s3, s37
	s_cselect_b32 s6, s7, s6
	s_cselect_b32 s3, s14, s3
	s_add_i32 s7, s6, 1
	s_cmp_ge_u32 s3, s37
	s_cselect_b32 s3, s7, s6
	s_xor_b32 s3, s3, s2
	s_sub_i32 s2, s3, s2
	s_mul_i32 s3, s2, s37
	s_sub_i32 s3, s36, s3
	s_lshl_b32 s2, s2, 6
	v_lshl_or_b32 v34, s3, 5, v98
	s_add_i32 s3, s76, -1
	v_or_b32_e32 v35, s2, v99
	s_ashr_i32 s2, s2, 31
	v_min_i32_e32 v34, s3, v34
	s_mul_i32 s6, s2, s76
	v_mad_u64_u32 v[36:37], s[2:3], v35, s76, 0
	v_add_u32_e32 v37, s6, v37
	v_lshl_add_u64 v[36:37], v[36:37], 2, s[4:5]
	v_ashrrev_i32_e32 v35, 31, v34
	v_lshl_add_u64 v[36:37], v[34:35], 2, v[36:37]
	s_lshl_b64 s[4:5], s[76:77], 3
	global_load_dword v34, v[36:37], off nt
	v_lshl_add_u64 v[36:37], v[36:37], 0, s[4:5]
	v_lshl_add_u64 v[38:39], v[36:37], 0, s[4:5]
	global_load_dword v35, v[36:37], off nt
	s_nop 0
	global_load_dword v36, v[38:39], off nt
	v_lshl_add_u64 v[38:39], v[38:39], 0, s[4:5]
	v_lshl_add_u64 v[40:41], v[38:39], 0, s[4:5]
	global_load_dword v37, v[38:39], off nt
	s_nop 0
	global_load_dword v38, v[40:41], off nt
	v_lshl_add_u64 v[40:41], v[40:41], 0, s[4:5]
	v_lshl_add_u64 v[42:43], v[40:41], 0, s[4:5]
	global_load_dword v39, v[40:41], off nt
	s_nop 0
	global_load_dword v40, v[42:43], off nt
	v_lshl_add_u64 v[42:43], v[42:43], 0, s[4:5]
	v_lshl_add_u64 v[44:45], v[42:43], 0, s[4:5]
	global_load_dword v41, v[42:43], off nt
	s_nop 0
	global_load_dword v42, v[44:45], off nt
	v_lshl_add_u64 v[44:45], v[44:45], 0, s[4:5]
	v_lshl_add_u64 v[46:47], v[44:45], 0, s[4:5]
	global_load_dword v43, v[44:45], off nt
	s_nop 0
	global_load_dword v44, v[46:47], off nt
	v_lshl_add_u64 v[46:47], v[46:47], 0, s[4:5]
	v_lshl_add_u64 v[48:49], v[46:47], 0, s[4:5]
	global_load_dword v45, v[46:47], off nt
	s_nop 0
	global_load_dword v46, v[48:49], off nt
	v_lshl_add_u64 v[48:49], v[48:49], 0, s[4:5]
	v_lshl_add_u64 v[50:51], v[48:49], 0, s[4:5]
	global_load_dword v47, v[48:49], off nt
	s_nop 0
	global_load_dword v48, v[50:51], off nt
	v_lshl_add_u64 v[50:51], v[50:51], 0, s[4:5]
	v_lshl_add_u64 v[52:53], v[50:51], 0, s[4:5]
	global_load_dword v49, v[50:51], off nt
	s_nop 0
	global_load_dword v50, v[52:53], off nt
	v_lshl_add_u64 v[52:53], v[52:53], 0, s[4:5]
	v_lshl_add_u64 v[54:55], v[52:53], 0, s[4:5]
	global_load_dword v51, v[52:53], off nt
	s_nop 0
	global_load_dword v52, v[54:55], off nt
	v_lshl_add_u64 v[54:55], v[54:55], 0, s[4:5]
	v_lshl_add_u64 v[56:57], v[54:55], 0, s[4:5]
	global_load_dword v53, v[54:55], off nt
	s_nop 0
	global_load_dword v54, v[56:57], off nt
	v_lshl_add_u64 v[56:57], v[56:57], 0, s[4:5]
	v_lshl_add_u64 v[58:59], v[56:57], 0, s[4:5]
	global_load_dword v55, v[56:57], off nt
	s_nop 0
	global_load_dword v56, v[58:59], off nt
	v_lshl_add_u64 v[58:59], v[58:59], 0, s[4:5]
	v_lshl_add_u64 v[60:61], v[58:59], 0, s[4:5]
	global_load_dword v57, v[58:59], off nt
	s_nop 0
	global_load_dword v58, v[60:61], off nt
	v_lshl_add_u64 v[60:61], v[60:61], 0, s[4:5]
	v_lshl_add_u64 v[62:63], v[60:61], 0, s[4:5]
	global_load_dword v59, v[60:61], off nt
	s_nop 0
	global_load_dword v60, v[62:63], off nt
	v_lshl_add_u64 v[62:63], v[62:63], 0, s[4:5]
	v_lshl_add_u64 v[64:65], v[62:63], 0, s[4:5]
	global_load_dword v61, v[62:63], off nt
	s_nop 0
	global_load_dword v62, v[64:65], off nt
	v_lshl_add_u64 v[64:65], v[64:65], 0, s[4:5]
	s_waitcnt lgkmcnt(0)
	v_lshl_add_u64 v[82:83], v[64:65], 0, s[4:5]
	global_load_dword v63, v[64:65], off nt
	s_nop 0
	global_load_dword v64, v[82:83], off nt
	v_lshl_add_u64 v[82:83], v[82:83], 0, s[4:5]
	global_load_dword v65, v[82:83], off nt
	s_abs_i32 s2, s29
	s_waitcnt lgkmcnt(0)
	v_cvt_f32_u32_e32 v82, s2
	s_sub_i32 s5, 0, s2
	s_abs_i32 s4, s28
	s_xor_b32 s3, s28, s29
	v_rcp_iflag_f32_e32 v82, v82
	s_ashr_i32 s3, s3, 31
	s_waitcnt vmcnt(62)
	ds_write2_b32 v109, v2, v3 offset1:66
	s_waitcnt vmcnt(60)
	ds_write2_b32 v109, v4, v5 offset0:132 offset1:198
	v_mul_f32_e32 v82, 0x4f7ffffe, v82
	v_cvt_u32_f32_e32 v82, v82
	s_nop 0
	v_readfirstlane_b32 s6, v82
	s_mul_i32 s5, s5, s6
	s_mul_hi_u32 s5, s6, s5
	s_add_i32 s6, s6, s5
	s_mul_hi_u32 s5, s4, s6
	s_mul_i32 s6, s5, s2
	s_sub_i32 s4, s4, s6
	s_add_i32 s7, s5, 1
	s_sub_i32 s6, s4, s2
	s_cmp_ge_u32 s4, s2
	v_add_u32_e32 v82, 0x400, v109
	s_cselect_b32 s5, s7, s5
	s_waitcnt vmcnt(58)
	ds_write2_b32 v82, v6, v7 offset0:8 offset1:74
	s_waitcnt vmcnt(56)
	ds_write2_b32 v82, v8, v9 offset0:140 offset1:206
	v_add_u32_e32 v82, 0x800, v109
	s_cselect_b32 s4, s6, s4
	s_add_i32 s6, s5, 1
	s_waitcnt vmcnt(54)
	ds_write2_b32 v82, v10, v11 offset0:16 offset1:82
	s_waitcnt vmcnt(52)
	ds_write2_b32 v82, v12, v13 offset0:148 offset1:214
	v_add_u32_e32 v82, 0xc00, v109
	s_cmp_ge_u32 s4, s2
	s_waitcnt vmcnt(50)
	ds_write2_b32 v82, v14, v15 offset0:24 offset1:90
	s_waitcnt vmcnt(48)
	ds_write2_b32 v82, v16, v17 offset0:156 offset1:222
	v_add_u32_e32 v82, 0x1000, v109
	s_cselect_b32 s2, s6, s5
	s_waitcnt vmcnt(46)
	ds_write2_b32 v82, v18, v19 offset0:32 offset1:98
	s_waitcnt vmcnt(44)
	ds_write2_b32 v82, v20, v21 offset0:164 offset1:230
	v_add_u32_e32 v82, 0x1400, v109
	s_xor_b32 s2, s2, s3
	s_waitcnt vmcnt(42)
	ds_write2_b32 v82, v22, v23 offset0:40 offset1:106
	s_waitcnt vmcnt(40)
	ds_write2_b32 v82, v24, v25 offset0:172 offset1:238
	v_add_u32_e32 v82, 0x1800, v109
	s_sub_i32 s2, s2, s3
	s_waitcnt vmcnt(38)
	ds_write2_b32 v82, v26, v27 offset0:48 offset1:114
	s_waitcnt vmcnt(36)
	ds_write2_b32 v82, v28, v29 offset0:180 offset1:246
	v_add_u32_e32 v82, 0x1c00, v109
	s_mul_i32 s3, s2, s29
	s_waitcnt vmcnt(34)
	ds_write2_b32 v82, v30, v31 offset0:56 offset1:122
	s_waitcnt vmcnt(32)
	ds_write2_b32 v82, v32, v33 offset0:188 offset1:254
	s_branch .Lcv_cont_2702

.Lcv_cont_2702:
	s_sub_i32 s15, s28, s3
	s_waitcnt lgkmcnt(0)
	s_lshl_b32 s14, s2, 6
	s_lshl_b32 s2, s15, 5
	s_bitcmp0_b32 s15, 3
	s_movk_i32 s3, 0x400
	s_cselect_b32 s3, s3, 0xc00
	s_cmp_gt_i32 s31, 1
	s_mov_b64 s[4:5], -1
	s_cbranch_scc1 .LBB0_2796
	ds_read2_b32 v[90:91], v102 offset1:33
	ds_read2_b32 v[88:89], v102 offset0:66 offset1:99
	ds_read2_b32 v[86:87], v102 offset0:132 offset1:165
	ds_read2_b32 v[84:85], v102 offset0:198 offset1:231
	s_cmp_lg_u32 s31, 1
	v_or_b32_e32 v93, s2, v100
	s_cselect_b64 s[6:7], -1, 0
	s_cmp_eq_u32 s31, 1
	s_cselect_b64 s[4:5], -1, 0
	v_cmp_lt_i32_e32 vcc, s46, v93
	s_and_b64 s[16:17], s[4:5], vcc
	v_mov_b32_e32 v92, v93
	s_and_saveexec_b64 s[4:5], s[16:17]
	s_cbranch_execz .LBB0_2724
	s_cmpk_gt_u32 s2, 0x9ff
	s_mov_b64 s[16:17], -1
	s_cbranch_scc0 .LBB0_2722
	s_cmpk_gt_u32 s2, 0xa2f
	s_cbranch_scc0 .LBB0_2719
	s_cmpk_gt_u32 s2, 0xe2f
	s_cbranch_scc0 .LBB0_2716
	s_cmpk_gt_u32 s2, 0x122f
	s_cbranch_scc0 .LBB0_2713
	s_cmpk_gt_u32 s2, 0x1237
	s_cbranch_scc0 .LBB0_2710
	v_add_u32_e32 v92, 0xc8, v93
	s_mov_b64 s[16:17], 0

.LBB0_2852:
	s_waitcnt lgkmcnt(0)
	s_andn2_b64 vcc, exec, s[10:11]
	s_cbranch_vccnz .LBB0_2650
	s_waitcnt vmcnt(0)
	v_mov_b64_e32 v[2:3], v[34:35]
	s_mov_b32 s29, s37
	s_mov_b32 s28, s36
	s_mov_b32 s31, s39
	s_mov_b32 s30, s38
	s_mov_b64 s[0:1], s[12:13]
	s_mov_b32 s34, s76
	v_mov_b64_e32 v[4:5], v[36:37]
	v_mov_b64_e32 v[6:7], v[38:39]
	v_mov_b64_e32 v[8:9], v[40:41]
	v_mov_b64_e32 v[10:11], v[42:43]
	v_mov_b64_e32 v[12:13], v[44:45]
	v_mov_b64_e32 v[14:15], v[46:47]
	v_mov_b64_e32 v[16:17], v[48:49]
	v_mov_b64_e32 v[18:19], v[50:51]
	v_mov_b64_e32 v[20:21], v[52:53]
	v_mov_b64_e32 v[22:23], v[54:55]
	v_mov_b64_e32 v[24:25], v[56:57]
	v_mov_b64_e32 v[26:27], v[58:59]
	v_mov_b64_e32 v[28:29], v[60:61]
	v_mov_b64_e32 v[30:31], v[62:63]
	v_mov_b64_e32 v[32:33], v[64:65]
	s_mov_b32 s27, s35
	s_branch .LBB0_2650

.LBB0_3090:
	v_cvt_f32_u32_e32 v34, s80
	s_sub_i32 s8, 0, s80
	s_abs_i32 s7, s82
	s_ashr_i32 s6, s82, 31
	v_rcp_iflag_f32_e32 v34, v34
	s_nop 0
	v_mul_f32_e32 v34, 0x4f7ffffe, v34
	v_cvt_u32_f32_e32 v34, v34
	s_nop 0
	v_readfirstlane_b32 s9, v34
	s_mul_i32 s8, s8, s9
	s_mul_hi_u32 s8, s9, s8
	s_add_i32 s9, s9, s8
	s_mul_hi_u32 s8, s7, s9
	s_mul_i32 s9, s8, s80
	s_sub_i32 s7, s7, s9
	s_add_i32 s9, s8, 1
	s_sub_i32 s10, s7, s80
	s_cmp_ge_u32 s7, s80
	s_cselect_b32 s8, s9, s8
	s_cselect_b32 s7, s10, s7
	s_add_i32 s9, s8, 1
	s_cmp_ge_u32 s7, s80
	s_cselect_b32 s7, s9, s8
	s_xor_b32 s7, s7, s6
	s_sub_i32 s6, s7, s6
	s_mul_i32 s7, s6, s80
	s_sub_i32 s7, s82, s7
	s_lshl_b32 s6, s6, 6
	v_lshl_or_b32 v34, s7, 5, v84
	s_add_i32 s7, s58, -1
	v_or_b32_e32 v35, s6, v85
	s_ashr_i32 s6, s6, 31
	v_min_i32_e32 v34, s7, v34
	s_mul_i32 s8, s6, s58
	v_mad_u64_u32 v[36:37], s[6:7], v35, s58, 0
	v_add_u32_e32 v37, s8, v37
	v_lshl_add_u64 v[36:37], v[36:37], 2, s[4:5]
	v_ashrrev_i32_e32 v35, 31, v34
	v_lshl_add_u64 v[36:37], v[34:35], 2, v[36:37]
	s_lshl_b64 s[4:5], s[58:59], 3
	global_load_dword v34, v[36:37], off nt
	v_lshl_add_u64 v[36:37], v[36:37], 0, s[4:5]
	v_lshl_add_u64 v[38:39], v[36:37], 0, s[4:5]
	global_load_dword v35, v[36:37], off nt
	s_nop 0
	global_load_dword v36, v[38:39], off nt
	v_lshl_add_u64 v[38:39], v[38:39], 0, s[4:5]
	v_lshl_add_u64 v[40:41], v[38:39], 0, s[4:5]
	global_load_dword v37, v[38:39], off nt
	s_nop 0
	global_load_dword v38, v[40:41], off nt
	v_lshl_add_u64 v[40:41], v[40:41], 0, s[4:5]
	v_lshl_add_u64 v[42:43], v[40:41], 0, s[4:5]
	global_load_dword v39, v[40:41], off nt
	s_nop 0
	global_load_dword v40, v[42:43], off nt
	v_lshl_add_u64 v[42:43], v[42:43], 0, s[4:5]
	v_lshl_add_u64 v[44:45], v[42:43], 0, s[4:5]
	global_load_dword v41, v[42:43], off nt
	s_nop 0
	global_load_dword v42, v[44:45], off nt
	v_lshl_add_u64 v[44:45], v[44:45], 0, s[4:5]
	v_lshl_add_u64 v[46:47], v[44:45], 0, s[4:5]
	global_load_dword v43, v[44:45], off nt
	s_nop 0
	global_load_dword v44, v[46:47], off nt
	v_lshl_add_u64 v[46:47], v[46:47], 0, s[4:5]
	v_lshl_add_u64 v[48:49], v[46:47], 0, s[4:5]
	global_load_dword v45, v[46:47], off nt
	s_nop 0
	global_load_dword v46, v[48:49], off nt
	v_lshl_add_u64 v[48:49], v[48:49], 0, s[4:5]
	v_lshl_add_u64 v[50:51], v[48:49], 0, s[4:5]
	global_load_dword v47, v[48:49], off nt
	s_nop 0
	global_load_dword v48, v[50:51], off nt
	v_lshl_add_u64 v[50:51], v[50:51], 0, s[4:5]
	v_lshl_add_u64 v[52:53], v[50:51], 0, s[4:5]
	global_load_dword v49, v[50:51], off nt
	s_nop 0
	global_load_dword v50, v[52:53], off nt
	v_lshl_add_u64 v[52:53], v[52:53], 0, s[4:5]
	v_lshl_add_u64 v[54:55], v[52:53], 0, s[4:5]
	global_load_dword v51, v[52:53], off nt
	s_nop 0
	global_load_dword v52, v[54:55], off nt
	v_lshl_add_u64 v[54:55], v[54:55], 0, s[4:5]
	v_lshl_add_u64 v[56:57], v[54:55], 0, s[4:5]
	global_load_dword v53, v[54:55], off nt
	s_nop 0
	global_load_dword v54, v[56:57], off nt
	v_lshl_add_u64 v[56:57], v[56:57], 0, s[4:5]
	v_lshl_add_u64 v[58:59], v[56:57], 0, s[4:5]
	global_load_dword v55, v[56:57], off nt
	s_nop 0
	global_load_dword v56, v[58:59], off nt
	v_lshl_add_u64 v[58:59], v[58:59], 0, s[4:5]
	v_lshl_add_u64 v[60:61], v[58:59], 0, s[4:5]
	global_load_dword v57, v[58:59], off nt
	s_nop 0
	global_load_dword v58, v[60:61], off nt
	v_lshl_add_u64 v[60:61], v[60:61], 0, s[4:5]
	v_lshl_add_u64 v[62:63], v[60:61], 0, s[4:5]
	global_load_dword v59, v[60:61], off nt
	s_nop 0
	global_load_dword v60, v[62:63], off nt
	v_lshl_add_u64 v[62:63], v[62:63], 0, s[4:5]
	v_lshl_add_u64 v[64:65], v[62:63], 0, s[4:5]
	global_load_dword v61, v[62:63], off nt
	s_nop 0
	global_load_dword v62, v[64:65], off nt
	v_lshl_add_u64 v[64:65], v[64:65], 0, s[4:5]
	s_waitcnt lgkmcnt(0)
	v_lshl_add_u64 v[68:69], v[64:65], 0, s[4:5]
	global_load_dword v63, v[64:65], off nt
	s_nop 0
	global_load_dword v64, v[68:69], off nt
	v_lshl_add_u64 v[68:69], v[68:69], 0, s[4:5]
	global_load_dword v65, v[68:69], off nt
	s_abs_i32 s4, s24
	s_waitcnt lgkmcnt(0)
	v_cvt_f32_u32_e32 v68, s4
	s_sub_i32 s7, 0, s4
	s_abs_i32 s6, s86
	s_xor_b32 s5, s86, s24
	v_rcp_iflag_f32_e32 v68, v68
	s_ashr_i32 s5, s5, 31
	s_waitcnt vmcnt(62)
	ds_write2_b32 v95, v2, v3 offset1:66
	s_waitcnt vmcnt(60)
	ds_write2_b32 v95, v4, v5 offset0:132 offset1:198
	v_mul_f32_e32 v68, 0x4f7ffffe, v68
	v_cvt_u32_f32_e32 v68, v68
	s_nop 0
	v_readfirstlane_b32 s8, v68
	s_mul_i32 s7, s7, s8
	s_mul_hi_u32 s7, s8, s7
	s_add_i32 s8, s8, s7
	s_mul_hi_u32 s7, s6, s8
	s_mul_i32 s8, s7, s4
	s_sub_i32 s6, s6, s8
	s_add_i32 s9, s7, 1
	s_sub_i32 s8, s6, s4
	s_cmp_ge_u32 s6, s4
	v_add_u32_e32 v68, 0x400, v95
	s_cselect_b32 s7, s9, s7
	s_waitcnt vmcnt(58)
	ds_write2_b32 v68, v6, v7 offset0:8 offset1:74
	s_waitcnt vmcnt(56)
	ds_write2_b32 v68, v8, v9 offset0:140 offset1:206
	v_add_u32_e32 v68, 0x800, v95
	s_cselect_b32 s6, s8, s6
	s_add_i32 s8, s7, 1
	s_waitcnt vmcnt(54)
	ds_write2_b32 v68, v10, v11 offset0:16 offset1:82
	s_waitcnt vmcnt(52)
	ds_write2_b32 v68, v12, v13 offset0:148 offset1:214
	v_add_u32_e32 v68, 0xc00, v95
	s_cmp_ge_u32 s6, s4
	s_waitcnt vmcnt(50)
	ds_write2_b32 v68, v14, v15 offset0:24 offset1:90
	s_waitcnt vmcnt(48)
	ds_write2_b32 v68, v16, v17 offset0:156 offset1:222
	v_add_u32_e32 v68, 0x1000, v95
	s_cselect_b32 s4, s8, s7
	s_waitcnt vmcnt(46)
	ds_write2_b32 v68, v18, v19 offset0:32 offset1:98
	s_waitcnt vmcnt(44)
	ds_write2_b32 v68, v20, v21 offset0:164 offset1:230
	v_add_u32_e32 v68, 0x1400, v95
	s_xor_b32 s4, s4, s5
	s_waitcnt vmcnt(42)
	ds_write2_b32 v68, v22, v23 offset0:40 offset1:106
	s_waitcnt vmcnt(40)
	ds_write2_b32 v68, v24, v25 offset0:172 offset1:238
	v_add_u32_e32 v68, 0x1800, v95
	s_sub_i32 s4, s4, s5
	s_waitcnt vmcnt(38)
	ds_write2_b32 v68, v26, v27 offset0:48 offset1:114
	s_waitcnt vmcnt(36)
	ds_write2_b32 v68, v28, v29 offset0:180 offset1:246
	v_add_u32_e32 v68, 0x1c00, v95
	s_mul_i32 s5, s4, s24
	s_waitcnt vmcnt(34)
	ds_write2_b32 v68, v30, v31 offset0:56 offset1:122
	s_waitcnt vmcnt(32)
	ds_write2_b32 v68, v32, v33 offset0:188 offset1:254
	s_branch .Lcv_cont_3091

.Lcv_cont_3091:
	s_sub_i32 s9, s86, s5
	s_waitcnt lgkmcnt(0)
	s_lshl_b32 s68, s4, 6
	s_lshl_b32 s27, s9, 5
	s_bitcmp0_b32 s9, 3
	s_movk_i32 s4, 0x400
	s_cselect_b32 s8, s4, 0xc00
	s_cmp_gt_i32 s84, 1
	s_mov_b64 s[4:5], -1
	s_cbranch_scc1 .LBB0_3185
	ds_read2_b32 v[76:77], v88 offset1:33
	ds_read2_b32 v[74:75], v88 offset0:66 offset1:99
	ds_read2_b32 v[72:73], v88 offset0:132 offset1:165
	ds_read2_b32 v[70:71], v88 offset0:198 offset1:231
	s_cmp_lg_u32 s84, 1
	v_or_b32_e32 v79, s27, v86
	s_cselect_b64 s[6:7], -1, 0
	s_cmp_eq_u32 s84, 1
	s_cselect_b64 s[4:5], -1, 0
	v_cmp_lt_i32_e32 vcc, s93, v79
	s_and_b64 s[10:11], s[4:5], vcc
	v_mov_b32_e32 v78, v79
	s_and_saveexec_b64 s[4:5], s[10:11]
	s_cbranch_execz .LBB0_3113
	s_cmpk_gt_u32 s27, 0x9ff
	s_mov_b64 s[70:71], -1
	s_cbranch_scc0 .LBB0_3111
	s_cmpk_gt_u32 s27, 0xa2f
	s_cbranch_scc0 .LBB0_3108
	s_cmpk_gt_u32 s27, 0xe2f
	s_cbranch_scc0 .LBB0_3105
	s_cmpk_gt_u32 s27, 0x122f
	s_cbranch_scc0 .LBB0_3102
	s_cmpk_gt_u32 s27, 0x1237
	s_cbranch_scc0 .LBB0_3099
	v_add_u32_e32 v78, 0xc8, v79
	s_mov_b64 s[70:71], 0

.LBB0_3241:
	s_waitcnt lgkmcnt(0)
	s_andn2_b64 vcc, exec, s[64:65]
	s_cbranch_vccnz .LBB0_3039
	s_waitcnt vmcnt(0)
	v_mov_b64_e32 v[2:3], v[34:35]
	s_mov_b32 s24, s80
	s_mov_b32 s86, s82
	s_mov_b32 s84, s26
	s_mov_b32 s81, s25
	s_mov_b64 s[60:61], s[66:67]
	s_mov_b32 s85, s58
	v_mov_b64_e32 v[4:5], v[36:37]
	v_mov_b64_e32 v[6:7], v[38:39]
	v_mov_b64_e32 v[8:9], v[40:41]
	v_mov_b64_e32 v[10:11], v[42:43]
	v_mov_b64_e32 v[12:13], v[44:45]
	v_mov_b64_e32 v[14:15], v[46:47]
	v_mov_b64_e32 v[16:17], v[48:49]
	v_mov_b64_e32 v[18:19], v[50:51]
	v_mov_b64_e32 v[20:21], v[52:53]
	v_mov_b64_e32 v[22:23], v[54:55]
	v_mov_b64_e32 v[24:25], v[56:57]
	v_mov_b64_e32 v[26:27], v[58:59]
	v_mov_b64_e32 v[28:29], v[60:61]
	v_mov_b64_e32 v[30:31], v[62:63]
	v_mov_b64_e32 v[32:33], v[64:65]
	s_mov_b32 s87, s83
	s_branch .LBB0_3039
